# speedup vs baseline: 1.0094x; 1.0094x over previous
.LBB0_60:
	s_andn2_b64 vcc, exec, s[4:5]
	s_cbranch_vccnz .LBB0_98
	s_cmpk_gt_u32 s2, 244
	s_cbranch_scc1 .LBB0_98
	s_load_dwordx2 s[4:5], s[0:1], 0x0
	s_load_dwordx4 s[12:15], s[0:1], 0x30
	s_lshl_b32 s3, s2, 12
	v_lshlrev_b32_e32 v1, 2, v0
	v_mov_b32_e32 v2, 0
	ds_write_b32 v1, v2
	v_or_b32_e32 v3, s3, v0
	s_mov_b32 s10, 0xf423f
	s_waitcnt lgkmcnt(0)
	s_add_u32 s6, s4, 0x3d0900
	s_addc_u32 s7, s5, 0
	v_min_u32_e32 v4, s10, v3
	v_lshlrev_b32_e32 v4, 2, v4
	global_load_dword v16, v4, s[6:7] nt
	global_load_dword v32, v4, s[4:5] nt
	v_add_u32_e32 v5, 1024, v3
	v_min_u32_e32 v5, s10, v5
	v_lshlrev_b32_e32 v5, 2, v5
	global_load_dword v17, v5, s[6:7] nt
	global_load_dword v33, v5, s[4:5] nt
	v_add_u32_e32 v6, 2048, v3
	v_min_u32_e32 v6, s10, v6
	v_lshlrev_b32_e32 v6, 2, v6
	global_load_dword v18, v6, s[6:7] nt
	global_load_dword v34, v6, s[4:5] nt
	v_add_u32_e32 v7, 3072, v3
	v_min_u32_e32 v7, s10, v7
	v_lshlrev_b32_e32 v7, 2, v7
	global_load_dword v19, v7, s[6:7] nt
	global_load_dword v35, v7, s[4:5] nt
	s_barrier
	s_mov_b32 s11, 0x5397829d
	s_mov_b32 s10, 0xf4240
	v_mov_b32_e32 v8, 0xffc
	s_waitcnt vmcnt(0)
	v_cmp_gt_u32_e32 vcc, s10, v3
	v_mul_hi_u32 v4, v16, s11
	v_lshrrev_b32_e32 v4, 5, v4
	v_mul_u32_u24_e32 v5, 0x62, v4
	v_sub_u32_e32 v5, v16, v5
	v_lshl_or_b32 v32, v5, 17, v32
	v_lshlrev_b32_e32 v4, 2, v4
	v_cndmask_b32_e32 v16, v8, v4, vcc
	v_add_u32_e32 v6, 1024, v3
	v_cmp_gt_u32_e32 vcc, s10, v6
	v_mul_hi_u32 v4, v17, s11
	v_lshrrev_b32_e32 v4, 5, v4
	v_mul_u32_u24_e32 v5, 0x62, v4
	v_sub_u32_e32 v5, v17, v5
	v_lshl_or_b32 v33, v5, 17, v33
	v_lshlrev_b32_e32 v4, 2, v4
	v_cndmask_b32_e32 v17, v8, v4, vcc
	v_add_u32_e32 v6, 2048, v3
	v_cmp_gt_u32_e32 vcc, s10, v6
	v_mul_hi_u32 v4, v18, s11
	v_lshrrev_b32_e32 v4, 5, v4
	v_mul_u32_u24_e32 v5, 0x62, v4
	v_sub_u32_e32 v5, v18, v5
	v_lshl_or_b32 v34, v5, 17, v34
	v_lshlrev_b32_e32 v4, 2, v4
	v_cndmask_b32_e32 v18, v8, v4, vcc
	v_add_u32_e32 v6, 3072, v3
	v_cmp_gt_u32_e32 vcc, s10, v6
	v_mul_hi_u32 v4, v19, s11
	v_lshrrev_b32_e32 v4, 5, v4
	v_mul_u32_u24_e32 v5, 0x62, v4
	v_sub_u32_e32 v5, v19, v5
	v_lshl_or_b32 v35, v5, 17, v35
	v_lshlrev_b32_e32 v4, 2, v4
	v_cndmask_b32_e32 v19, v8, v4, vcc
	v_mov_b32_e32 v7, 1
	ds_add_rtn_u32 v48, v16, v7
	ds_add_rtn_u32 v49, v17, v7
	ds_add_rtn_u32 v50, v18, v7
	ds_add_rtn_u32 v51, v19, v7
	s_waitcnt lgkmcnt(0)
	s_barrier
	ds_read_b32 v4, v1
	v_and_b32_e32 v8, 63, v0
	v_lshrrev_b32_e32 v9, 6, v0
	s_waitcnt lgkmcnt(0)
	v_add_u32_dpp v5, v4, v4 row_shr:1 row_mask:0xf bank_mask:0xf bound_ctrl:1
	s_nop 1
	v_add_u32_dpp v5, v5, v5 row_shr:2 row_mask:0xf bank_mask:0xf bound_ctrl:1
	s_nop 1
	v_add_u32_dpp v5, v5, v5 row_shr:4 row_mask:0xf bank_mask:0xf bound_ctrl:1
	s_nop 1
	v_add_u32_dpp v5, v5, v5 row_shr:8 row_mask:0xf bank_mask:0xf bound_ctrl:1
	s_nop 1
	v_add_u32_dpp v5, v5, v5 row_bcast:15 row_mask:0xa bank_mask:0xf
	s_nop 1
	v_add_u32_dpp v5, v5, v5 row_bcast:31 row_mask:0xc bank_mask:0xf
	v_readfirstlane_b32 s9, v9
	s_nop 0
	v_readlane_b32 s8, v5, 63
	s_lshl_b32 s16, s9, 2
	v_mov_b32_e32 v10, s16
	s_nop 1
	v_mov_b32_e32 v11, s8
	ds_write_b32 v10, v11 offset:4096
	s_waitcnt lgkmcnt(0)
	s_barrier
	v_min_u32_e32 v10, 15, v8
	v_lshlrev_b32_e32 v10, 2, v10
	ds_read_b32 v11, v10 offset:4096
	v_cmp_gt_u32_e32 vcc, s9, v8
	v_sub_u32_e32 v5, v5, v4
	s_waitcnt lgkmcnt(0)
	v_cndmask_b32_e32 v11, 0, v11, vcc
	s_nop 1
	v_add_u32_dpp v11, v11, v11 row_shr:1 row_mask:0xf bank_mask:0xf bound_ctrl:1
	s_nop 1
	v_add_u32_dpp v11, v11, v11 row_shr:2 row_mask:0xf bank_mask:0xf bound_ctrl:1
	s_nop 1
	v_add_u32_dpp v11, v11, v11 row_shr:4 row_mask:0xf bank_mask:0xf bound_ctrl:1
	s_nop 1
	v_add_u32_dpp v11, v11, v11 row_shr:8 row_mask:0xf bank_mask:0xf bound_ctrl:1
	s_nop 1
	v_readlane_b32 s17, v11, 15
	s_nop 3
	v_add_u32_e32 v5, s17, v5
	ds_write_b32 v1, v5
	s_waitcnt lgkmcnt(0)
	s_barrier
	s_mulk_i32 s2, 0x3fe
	v_add_u32_e32 v10, s2, v0
	v_lshlrev_b32_e32 v10, 2, v10
	s_movk_i32 s16, 0x3fe
	v_cmp_gt_u32_e32 vcc, s16, v0
	s_and_saveexec_b64 s[8:9], vcc
	s_cbranch_execz .Lk1p_o
	global_store_dword v10, v5, s[14:15] sc1
.Lk1p_o:
	s_mov_b64 exec, s[8:9]
	ds_read_b32 v16, v16
	ds_read_b32 v17, v17
	ds_read_b32 v18, v18
	ds_read_b32 v19, v19
	s_waitcnt lgkmcnt(0)
	v_add_u32_e32 v4, v16, v48
	v_lshlrev_b32_e32 v4, 2, v4
	ds_write_b32 v4, v32 offset:4352
	v_add_u32_e32 v5, v17, v49
	v_lshlrev_b32_e32 v5, 2, v5
	ds_write_b32 v5, v33 offset:4352
	v_add_u32_e32 v6, v18, v50
	v_lshlrev_b32_e32 v6, 2, v6
	ds_write_b32 v6, v34 offset:4352
	v_add_u32_e32 v7, v19, v51
	v_lshlrev_b32_e32 v7, 2, v7
	ds_write_b32 v7, v35 offset:4352
	s_waitcnt lgkmcnt(0)
	s_barrier
	s_sub_u32 s16, 0xf4240, s3
	s_min_u32 s16, s16, 0x1000
	v_lshlrev_b32_e32 v4, 2, v0
	v_lshlrev_b32_e32 v5, 4, v0
	ds_read_b128 v[16:19], v5 offset:4352
	s_lshl_b32 s17, s3, 2
	v_add_u32_e32 v6, s17, v5
	v_cmp_gt_u32_e32 vcc, s16, v4
	s_waitcnt lgkmcnt(0)
	s_mov_b64 exec, vcc
	s_cbranch_execz .LBB0_98
	global_store_dwordx4 v6, v[16:19], s[12:13] sc1

	.amdhsa_kernel _Z6k_partPKiPKfS2_S2_S2_S2_PiS3_PDF16_S4_S4_
		.amdhsa_group_segment_fixed_size 20736
		.amdhsa_private_segment_fixed_size 0
		.amdhsa_kernarg_size 88
		.amdhsa_user_sgpr_count 2
		.amdhsa_user_sgpr_dispatch_ptr 0
		.amdhsa_user_sgpr_queue_ptr 0
		.amdhsa_user_sgpr_kernarg_segment_ptr 1
		.amdhsa_user_sgpr_dispatch_id 0
		.amdhsa_user_sgpr_kernarg_preload_length 0
		.amdhsa_user_sgpr_kernarg_preload_offset 0
		.amdhsa_user_sgpr_private_segment_size 0
		.amdhsa_uses_dynamic_stack 0
		.amdhsa_enable_private_segment 0
		.amdhsa_system_sgpr_workgroup_id_x 1
		.amdhsa_system_sgpr_workgroup_id_y 0
		.amdhsa_system_sgpr_workgroup_id_z 0
		.amdhsa_system_sgpr_workgroup_info 0
		.amdhsa_system_vgpr_workitem_id 0
		.amdhsa_next_free_vgpr 64
		.amdhsa_next_free_sgpr 22
		.amdhsa_accum_offset 64
		.amdhsa_reserve_vcc 1
		.amdhsa_float_round_mode_32 0
		.amdhsa_float_round_mode_16_64 0
		.amdhsa_float_denorm_mode_32 3
		.amdhsa_float_denorm_mode_16_64 3
		.amdhsa_dx10_clamp 1
		.amdhsa_ieee_mode 1
		.amdhsa_fp16_overflow 0
		.amdhsa_tg_split 0
		.amdhsa_exception_fp_ieee_invalid_op 0
		.amdhsa_exception_fp_denorm_src 0
		.amdhsa_exception_fp_ieee_div_zero 0
		.amdhsa_exception_fp_ieee_overflow 0
		.amdhsa_exception_fp_ieee_underflow 0
		.amdhsa_exception_fp_ieee_inexact 0
		.amdhsa_exception_int_div_zero 0
	.end_amdhsa_kernel

amdhsa.kernels:
  - .agpr_count:     0
    .args:
      - .actual_access:  read_only
        .address_space:  global
        .offset:         0
        .size:           8
        .value_kind:     global_buffer
      - .actual_access:  read_only
        .address_space:  global
        .offset:         8
        .size:           8
        .value_kind:     global_buffer
      - .actual_access:  read_only
        .address_space:  global
        .offset:         16
        .size:           8
        .value_kind:     global_buffer
      - .actual_access:  read_only
        .address_space:  global
        .offset:         24
        .size:           8
        .value_kind:     global_buffer
      - .actual_access:  read_only
        .address_space:  global
        .offset:         32
        .size:           8
        .value_kind:     global_buffer
      - .actual_access:  read_only
        .address_space:  global
        .offset:         40
        .size:           8
        .value_kind:     global_buffer
      - .actual_access:  write_only
        .address_space:  global
        .offset:         48
        .size:           8
        .value_kind:     global_buffer
      - .actual_access:  write_only
        .address_space:  global
        .offset:         56
        .size:           8
        .value_kind:     global_buffer
      - .actual_access:  write_only
        .address_space:  global
        .offset:         64
        .size:           8
        .value_kind:     global_buffer
      - .actual_access:  write_only
        .address_space:  global
        .offset:         72
        .size:           8
        .value_kind:     global_buffer
      - .actual_access:  write_only
        .address_space:  global
        .offset:         80
        .size:           8
        .value_kind:     global_buffer
    .group_segment_fixed_size: 20736
    .kernarg_segment_align: 8
    .kernarg_segment_size: 88
    .language:       OpenCL C
    .language_version:
      - 2
      - 0
    .max_flat_workgroup_size: 1024
    .name:           _Z6k_partPKiPKfS2_S2_S2_S2_PiS3_PDF16_S4_S4_
    .private_segment_fixed_size: 0
    .sgpr_count:     28
    .sgpr_spill_count: 0
    .symbol:         _Z6k_partPKiPKfS2_S2_S2_S2_PiS3_PDF16_S4_S4_.kd
    .uniform_work_group_size: 1
    .uses_dynamic_stack: false
    .vgpr_count:     64
    .vgpr_spill_count: 0
    .wavefront_size: 64
  - .agpr_count:     0
    .args:
      - .actual_access:  read_only
        .address_space:  global
        .offset:         0
        .size:           8
        .value_kind:     global_buffer
      - .actual_access:  read_only
        .address_space:  global
        .offset:         8
        .size:           8
        .value_kind:     global_buffer
      - .actual_access:  read_only
        .address_space:  global
        .offset:         16
        .size:           8
        .value_kind:     global_buffer
      - .actual_access:  write_only
        .address_space:  global
        .offset:         24
        .size:           8
        .value_kind:     global_buffer
      - .address_space:  global
        .offset:         32
        .size:           8
        .value_kind:     global_buffer
      - .actual_access:  read_only
        .address_space:  global
        .offset:         40
        .size:           8
        .value_kind:     global_buffer
      - .actual_access:  read_only
        .address_space:  global
        .offset:         48
        .size:           8
        .value_kind:     global_buffer
      - .actual_access:  read_only
        .address_space:  global
        .offset:         56
        .size:           8
        .value_kind:     global_buffer
      - .actual_access:  read_only
        .address_space:  global
        .offset:         64
        .size:           8
        .value_kind:     global_buffer
      - .actual_access:  write_only
        .address_space:  global
        .offset:         72
        .size:           8
        .value_kind:     global_buffer
      - .actual_access:  write_only
        .address_space:  global
        .offset:         80
        .size:           8
        .value_kind:     global_buffer
    .group_segment_fixed_size: 38832
    .kernarg_segment_align: 8
    .kernarg_segment_size: 88
    .language:       OpenCL C
    .language_version:
      - 2
      - 0
    .max_flat_workgroup_size: 512
    .name:           _Z8k_layer1PKDF16_PKiS2_PiS3_PKDv4_jS6_PKfS8_P15HIP_vector_typeIfLj2EESB_
    .private_segment_fixed_size: 0
    .sgpr_count:     76
    .sgpr_spill_count: 0
    .symbol:         _Z8k_layer1PKDF16_PKiS2_PiS3_PKDv4_jS6_PKfS8_P15HIP_vector_typeIfLj2EESB_.kd
    .uniform_work_group_size: 1
    .uses_dynamic_stack: false
    .vgpr_count:     64
    .vgpr_spill_count: 0
    .wavefront_size: 64
  - .agpr_count:     0
    .args:
      - .actual_access:  read_only
        .address_space:  global
        .offset:         0
        .size:           8
        .value_kind:     global_buffer
      - .actual_access:  read_only
        .address_space:  global
        .offset:         8
        .size:           8
        .value_kind:     global_buffer
      - .actual_access:  read_only
        .address_space:  global
        .offset:         16
        .size:           8
        .value_kind:     global_buffer
      - .actual_access:  read_only
        .address_space:  global
        .offset:         24
        .size:           8
        .value_kind:     global_buffer
      - .actual_access:  write_only
        .address_space:  global
        .offset:         32
        .size:           8
        .value_kind:     global_buffer
    .group_segment_fixed_size: 0
    .kernarg_segment_align: 8
    .kernarg_segment_size: 40
    .language:       OpenCL C
    .language_version:
      - 2
      - 0
    .max_flat_workgroup_size: 448
    .name:           _Z8k_layer2PK15HIP_vector_typeIfLj2EES2_PKiS4_PS0_
    .private_segment_fixed_size: 0
    .sgpr_count:     21
    .sgpr_spill_count: 0
    .symbol:         _Z8k_layer2PK15HIP_vector_typeIfLj2EES2_PKiS4_PS0_.kd
    .uniform_work_group_size: 1
    .uses_dynamic_stack: false
    .vgpr_count:     25
    .vgpr_spill_count: 0
    .wavefront_size: 64
